# v50 + final phase: rows with a slot in the split-K tail tiles request all their operand lines at once before the serialized generic loads
# baseline (speedup 1.0000x reference)
; #define GAS __attribute__((address_space(1)))
; __device__ __forceinline__ f32x4 y2_load(Frame& F, const bf16* Y2, size_t s, int col) {
;     f32x4 r;
;     if (s < (size_t)Y2_FULL_TILES * 256 * DM) { const v2u y = *(const GAS v2u*)(Y2 + s + col); r.x = bflo(y.x); r.y = bfhi(y.x); r.z = bflo(y.y); r.w = bfhi(y.y); }
;     else { const bf16* P = WSP(const bf16, WS_XN) + (s - (size_t)Y2_FULL_TILES * 256 * DM) + col; r = (f32x4){0.f, 0.f, 0.f, 0.f};
; #pragma unroll
;         for (int p = 0; p < 7; ++p) { const v2u y = *(const GAS v2u*)(P + (size_t)p * Y2_PART_ROWS * DM); r.x += bflo(y.x); r.y += bfhi(y.x); r.z += bflo(y.y); r.w += bfhi(y.y); } }
; __device__ __forceinline__ void final_phase(Frame& F) {
;     ...
;         const bool tail = __builtin_amdgcn_readfirstlane((int)((s0 >= (size_t)Y2_FULL_TILES * 256 * DM) | (s1 >= (size_t)Y2_FULL_TILES * 256 * DM))) != 0;
;         if (!tail) {
; #pragma unroll
;             for (int j = 0; j < 8; ++j) { const int col = 4 * (F.lane + 64 * j);
;                 const v2u ya = *(const GAS v2u*)(Y2 + s0 + col), yb = *(const GAS v2u*)(Y2 + s1 + col); const f32x4 gg = *(const GAS f32x4*)(g2 + col);
;                 f32x4 mo; mo.x = w0 * bflo(ya.x) + w1 * bflo(yb.x); mo.y = w0 * bfhi(ya.x) + w1 * bfhi(yb.x); mo.z = w0 * bflo(ya.y) + w1 * bflo(yb.y); mo.w = w0 * bfhi(ya.y) + w1 * bfhi(yb.y);
;                 { const v2u hw = hr[64 * j]; f32x4 hv; hv.x = bflo(hw.x); hv.y = bfhi(hw.x); hv.z = bflo(hw.y); hv.w = bfhi(hw.y); v[j] = hv + gg * mo; } s += (v[j].x * v[j].x + v[j].y * v[j].y) + (v[j].z * v[j].z + v[j].w * v[j].w); }
;         } else {
; #pragma unroll
;             for (int j = 0; j < 8; ++j) { const int col = 4 * (F.lane + 64 * j);
;                 const f32x4 fa = y2_load(F, Y2, s0, col), fb = y2_load(F, Y2, s1, col); const f32x4 gg = *(const GAS f32x4*)(g2 + col);
.LBB0_2193:
	s_andn2_b64 vcc, exec, s[2:3]
	s_cbranch_vccnz .LBB0_2190
	v_cmp_gt_u64_e64 s[2:3], s[4:5], v[62:63]
	s_lshl_b64 s[4:5], s[4:5], 1
	s_add_u32 s24, s42, s4
	s_addc_u32 s25, s43, s5
	s_add_u32 s20, s8, s4
	s_addc_u32 s21, s9, s5
	s_mov_b64 s[4:5], -1
	s_and_b64 vcc, exec, s[2:3]
	v_lshlrev_b32_e32 v28, 1, v30
	s_cmp_lg_u64 s[2:3], 0
	s_cselect_b32 s98, s24, s20
	s_cselect_b32 s99, s25, s21
	global_load_dwordx2 v[192:193], v28, s[98:99]
	global_load_dwordx2 v[192:193], v28, s[98:99] offset:512
	global_load_dwordx2 v[192:193], v28, s[98:99] offset:1024
	global_load_dwordx2 v[192:193], v28, s[98:99] offset:1536
	global_load_dwordx2 v[192:193], v28, s[98:99] offset:2048
	global_load_dwordx2 v[192:193], v28, s[98:99] offset:2560
	global_load_dwordx2 v[192:193], v28, s[98:99] offset:3072
	global_load_dwordx2 v[192:193], v28, s[98:99] offset:3584
	s_cmp_lg_u64 s[2:3], 0
	s_cbranch_scc0 .Lp19_pf_s1
	s_add_u32 s98, s98, 0x800000
	s_addc_u32 s99, s99, 0
	global_load_dwordx2 v[192:193], v28, s[98:99]
	global_load_dwordx2 v[192:193], v28, s[98:99] offset:512
	global_load_dwordx2 v[192:193], v28, s[98:99] offset:1024
	global_load_dwordx2 v[192:193], v28, s[98:99] offset:1536
	global_load_dwordx2 v[192:193], v28, s[98:99] offset:2048
	global_load_dwordx2 v[192:193], v28, s[98:99] offset:2560
	global_load_dwordx2 v[192:193], v28, s[98:99] offset:3072
	global_load_dwordx2 v[192:193], v28, s[98:99] offset:3584
	s_add_u32 s98, s98, 0x800000
	s_addc_u32 s99, s99, 0
	global_load_dwordx2 v[192:193], v28, s[98:99]
	global_load_dwordx2 v[192:193], v28, s[98:99] offset:512
	global_load_dwordx2 v[192:193], v28, s[98:99] offset:1024
	global_load_dwordx2 v[192:193], v28, s[98:99] offset:1536
	global_load_dwordx2 v[192:193], v28, s[98:99] offset:2048
	global_load_dwordx2 v[192:193], v28, s[98:99] offset:2560
	global_load_dwordx2 v[192:193], v28, s[98:99] offset:3072
	global_load_dwordx2 v[192:193], v28, s[98:99] offset:3584
	s_add_u32 s98, s98, 0x800000
	s_addc_u32 s99, s99, 0
	global_load_dwordx2 v[192:193], v28, s[98:99]
	global_load_dwordx2 v[192:193], v28, s[98:99] offset:512
	global_load_dwordx2 v[192:193], v28, s[98:99] offset:1024
	global_load_dwordx2 v[192:193], v28, s[98:99] offset:1536
	global_load_dwordx2 v[192:193], v28, s[98:99] offset:2048
	global_load_dwordx2 v[192:193], v28, s[98:99] offset:2560
	global_load_dwordx2 v[192:193], v28, s[98:99] offset:3072
	global_load_dwordx2 v[192:193], v28, s[98:99] offset:3584
	s_add_u32 s98, s98, 0x800000
	s_addc_u32 s99, s99, 0
	global_load_dwordx2 v[192:193], v28, s[98:99]
	global_load_dwordx2 v[192:193], v28, s[98:99] offset:512
	global_load_dwordx2 v[192:193], v28, s[98:99] offset:1024
	global_load_dwordx2 v[192:193], v28, s[98:99] offset:1536
	global_load_dwordx2 v[192:193], v28, s[98:99] offset:2048
	global_load_dwordx2 v[192:193], v28, s[98:99] offset:2560
	global_load_dwordx2 v[192:193], v28, s[98:99] offset:3072
	global_load_dwordx2 v[192:193], v28, s[98:99] offset:3584
	s_add_u32 s98, s98, 0x800000
	s_addc_u32 s99, s99, 0
	global_load_dwordx2 v[192:193], v28, s[98:99]
	global_load_dwordx2 v[192:193], v28, s[98:99] offset:512
	global_load_dwordx2 v[192:193], v28, s[98:99] offset:1024
	global_load_dwordx2 v[192:193], v28, s[98:99] offset:1536
	global_load_dwordx2 v[192:193], v28, s[98:99] offset:2048
	global_load_dwordx2 v[192:193], v28, s[98:99] offset:2560
	global_load_dwordx2 v[192:193], v28, s[98:99] offset:3072
	global_load_dwordx2 v[192:193], v28, s[98:99] offset:3584
	s_add_u32 s98, s98, 0x800000
	s_addc_u32 s99, s99, 0
	global_load_dwordx2 v[192:193], v28, s[98:99]
	global_load_dwordx2 v[192:193], v28, s[98:99] offset:512
	global_load_dwordx2 v[192:193], v28, s[98:99] offset:1024
	global_load_dwordx2 v[192:193], v28, s[98:99] offset:1536
	global_load_dwordx2 v[192:193], v28, s[98:99] offset:2048
	global_load_dwordx2 v[192:193], v28, s[98:99] offset:2560
	global_load_dwordx2 v[192:193], v28, s[98:99] offset:3072
	global_load_dwordx2 v[192:193], v28, s[98:99] offset:3584
; #define GAS __attribute__((address_space(1)))
; __device__ __forceinline__ f32x4 y2_load(Frame& F, const bf16* Y2, size_t s, int col) {
;     f32x4 r;
;     if (s < (size_t)Y2_FULL_TILES * 256 * DM) { const v2u y = *(const GAS v2u*)(Y2 + s + col); r.x = bflo(y.x); r.y = bfhi(y.x); r.z = bflo(y.y); r.w = bfhi(y.y); }
;     else { const bf16* P = WSP(const bf16, WS_XN) + (s - (size_t)Y2_FULL_TILES * 256 * DM) + col; r = (f32x4){0.f, 0.f, 0.f, 0.f};
; #pragma unroll
;         for (int p = 0; p < 7; ++p) { const v2u y = *(const GAS v2u*)(P + (size_t)p * Y2_PART_ROWS * DM); r.x += bflo(y.x); r.y += bfhi(y.x); r.z += bflo(y.y); r.w += bfhi(y.y); } }
;     return r;
; __device__ __forceinline__ void final_phase(Frame& F) {
;     ...
;         } else {
; #pragma unroll
;             for (int j = 0; j < 8; ++j) { const int col = 4 * (F.lane + 64 * j);
;                 const f32x4 fa = y2_load(F, Y2, s0, col), fb = y2_load(F, Y2, s1, col); const f32x4 gg = *(const GAS f32x4*)(g2 + col);
;                 const f32x4 mo = w0 * fa + w1 * fb;
.Lp19_pf_s1:
	s_lshl_b64 s[98:99], s[0:1], 1
	s_cmp_gt_u32 s0, 0x3ffffff
	s_cselect_b32 s100, s42, s8
	s_cselect_b32 s101, s43, s9
	s_add_u32 s98, s98, s100
	s_addc_u32 s99, s99, s101
	global_load_dwordx2 v[192:193], v28, s[98:99]
	global_load_dwordx2 v[192:193], v28, s[98:99] offset:512
	global_load_dwordx2 v[192:193], v28, s[98:99] offset:1024
	global_load_dwordx2 v[192:193], v28, s[98:99] offset:1536
	global_load_dwordx2 v[192:193], v28, s[98:99] offset:2048
	global_load_dwordx2 v[192:193], v28, s[98:99] offset:2560
	global_load_dwordx2 v[192:193], v28, s[98:99] offset:3072
	global_load_dwordx2 v[192:193], v28, s[98:99] offset:3584
	s_cmp_gt_u32 s0, 0x3ffffff
	s_cbranch_scc0 .Lp19_pf_done
	s_add_u32 s98, s98, 0x800000
	s_addc_u32 s99, s99, 0
	global_load_dwordx2 v[192:193], v28, s[98:99]
	global_load_dwordx2 v[192:193], v28, s[98:99] offset:512
	global_load_dwordx2 v[192:193], v28, s[98:99] offset:1024
	global_load_dwordx2 v[192:193], v28, s[98:99] offset:1536
	global_load_dwordx2 v[192:193], v28, s[98:99] offset:2048
	global_load_dwordx2 v[192:193], v28, s[98:99] offset:2560
	global_load_dwordx2 v[192:193], v28, s[98:99] offset:3072
	global_load_dwordx2 v[192:193], v28, s[98:99] offset:3584
	s_add_u32 s98, s98, 0x800000
	s_addc_u32 s99, s99, 0
	global_load_dwordx2 v[192:193], v28, s[98:99]
	global_load_dwordx2 v[192:193], v28, s[98:99] offset:512
	global_load_dwordx2 v[192:193], v28, s[98:99] offset:1024
	global_load_dwordx2 v[192:193], v28, s[98:99] offset:1536
	global_load_dwordx2 v[192:193], v28, s[98:99] offset:2048
	global_load_dwordx2 v[192:193], v28, s[98:99] offset:2560
	global_load_dwordx2 v[192:193], v28, s[98:99] offset:3072
	global_load_dwordx2 v[192:193], v28, s[98:99] offset:3584
	s_add_u32 s98, s98, 0x800000
	s_addc_u32 s99, s99, 0
	global_load_dwordx2 v[192:193], v28, s[98:99]
	global_load_dwordx2 v[192:193], v28, s[98:99] offset:512
	global_load_dwordx2 v[192:193], v28, s[98:99] offset:1024
	global_load_dwordx2 v[192:193], v28, s[98:99] offset:1536
	global_load_dwordx2 v[192:193], v28, s[98:99] offset:2048
	global_load_dwordx2 v[192:193], v28, s[98:99] offset:2560
	global_load_dwordx2 v[192:193], v28, s[98:99] offset:3072
	global_load_dwordx2 v[192:193], v28, s[98:99] offset:3584
	s_add_u32 s98, s98, 0x800000
	s_addc_u32 s99, s99, 0
	global_load_dwordx2 v[192:193], v28, s[98:99]
	global_load_dwordx2 v[192:193], v28, s[98:99] offset:512
	global_load_dwordx2 v[192:193], v28, s[98:99] offset:1024
	global_load_dwordx2 v[192:193], v28, s[98:99] offset:1536
	global_load_dwordx2 v[192:193], v28, s[98:99] offset:2048
	global_load_dwordx2 v[192:193], v28, s[98:99] offset:2560
	global_load_dwordx2 v[192:193], v28, s[98:99] offset:3072
	global_load_dwordx2 v[192:193], v28, s[98:99] offset:3584
	s_add_u32 s98, s98, 0x800000
	s_addc_u32 s99, s99, 0
	global_load_dwordx2 v[192:193], v28, s[98:99]
	global_load_dwordx2 v[192:193], v28, s[98:99] offset:512
	global_load_dwordx2 v[192:193], v28, s[98:99] offset:1024
	global_load_dwordx2 v[192:193], v28, s[98:99] offset:1536
	global_load_dwordx2 v[192:193], v28, s[98:99] offset:2048
	global_load_dwordx2 v[192:193], v28, s[98:99] offset:2560
	global_load_dwordx2 v[192:193], v28, s[98:99] offset:3072
	global_load_dwordx2 v[192:193], v28, s[98:99] offset:3584
	s_add_u32 s98, s98, 0x800000
	s_addc_u32 s99, s99, 0
	global_load_dwordx2 v[192:193], v28, s[98:99]
	global_load_dwordx2 v[192:193], v28, s[98:99] offset:512
	global_load_dwordx2 v[192:193], v28, s[98:99] offset:1024
	global_load_dwordx2 v[192:193], v28, s[98:99] offset:1536
	global_load_dwordx2 v[192:193], v28, s[98:99] offset:2048
	global_load_dwordx2 v[192:193], v28, s[98:99] offset:2560
	global_load_dwordx2 v[192:193], v28, s[98:99] offset:3072
	global_load_dwordx2 v[192:193], v28, s[98:99] offset:3584
.Lp19_pf_done:
	s_cbranch_vccz .LBB0_2196
	v_lshl_add_u64 v[0:1], s[24:25], 0, v[28:29]
	v_add_co_u32_e32 v4, vcc, 0x800000, v0
	global_load_dwordx2 v[2:3], v28, s[24:25]
	s_nop 0
	v_addc_co_u32_e32 v5, vcc, 0, v1, vcc
	v_add_co_u32_e32 v6, vcc, 0x1000000, v0
	global_load_dwordx2 v[4:5], v[4:5], off
	s_nop 0
	v_addc_co_u32_e32 v7, vcc, 0, v1, vcc
	v_add_co_u32_e32 v8, vcc, 0x1800000, v0
	global_load_dwordx2 v[6:7], v[6:7], off
	s_nop 0
	v_addc_co_u32_e32 v9, vcc, 0, v1, vcc
	v_add_co_u32_e32 v10, vcc, 0x2000000, v0
	global_load_dwordx2 v[8:9], v[8:9], off
	s_nop 0
	v_addc_co_u32_e32 v11, vcc, 0, v1, vcc
	v_add_co_u32_e32 v12, vcc, 0x2800000, v0
	global_load_dwordx2 v[10:11], v[10:11], off
	s_nop 0
	v_addc_co_u32_e32 v13, vcc, 0, v1, vcc
	v_add_co_u32_e32 v0, vcc, 0x3000000, v0
	global_load_dwordx2 v[12:13], v[12:13], off
	s_nop 0
	v_addc_co_u32_e32 v1, vcc, 0, v1, vcc
	global_load_dwordx2 v[0:1], v[0:1], off
	s_mov_b64 s[4:5], 0
	s_waitcnt vmcnt(6)
	v_lshlrev_b32_e32 v14, 16, v2
	v_and_b32_e32 v15, 0xffff0000, v2
	v_lshlrev_b32_e32 v2, 16, v3
	v_and_b32_e32 v3, 0xffff0000, v3
	v_pk_add_f32 v[14:15], v[14:15], 0 op_sel_hi:[1,0]
	v_pk_add_f32 v[2:3], v[2:3], 0 op_sel_hi:[1,0]
	s_waitcnt vmcnt(5)
	v_lshlrev_b32_e32 v16, 16, v4
	v_and_b32_e32 v17, 0xffff0000, v4
	v_lshlrev_b32_e32 v4, 16, v5
	v_and_b32_e32 v5, 0xffff0000, v5
	v_pk_add_f32 v[14:15], v[14:15], v[16:17]
	s_waitcnt vmcnt(4)
	v_lshlrev_b32_e32 v16, 16, v6
	v_and_b32_e32 v17, 0xffff0000, v6
	v_pk_add_f32 v[2:3], v[2:3], v[4:5]
	v_lshlrev_b32_e32 v4, 16, v7
	v_and_b32_e32 v5, 0xffff0000, v7
	v_pk_add_f32 v[6:7], v[14:15], v[16:17]
	s_waitcnt vmcnt(3)
	v_lshlrev_b32_e32 v14, 16, v8
	v_and_b32_e32 v15, 0xffff0000, v8
	v_pk_add_f32 v[2:3], v[2:3], v[4:5]
	v_lshlrev_b32_e32 v4, 16, v9
	v_and_b32_e32 v5, 0xffff0000, v9
	v_pk_add_f32 v[6:7], v[6:7], v[14:15]
	s_waitcnt vmcnt(2)
	v_lshlrev_b32_e32 v8, 16, v10
	v_and_b32_e32 v9, 0xffff0000, v10
	v_pk_add_f32 v[2:3], v[2:3], v[4:5]
	v_lshlrev_b32_e32 v4, 16, v11
	v_and_b32_e32 v5, 0xffff0000, v11
	v_pk_add_f32 v[6:7], v[6:7], v[8:9]
	s_waitcnt vmcnt(1)
	v_lshlrev_b32_e32 v8, 16, v12
	v_and_b32_e32 v9, 0xffff0000, v12
	v_pk_add_f32 v[2:3], v[2:3], v[4:5]
	v_lshlrev_b32_e32 v4, 16, v13
	v_and_b32_e32 v5, 0xffff0000, v13
	v_pk_add_f32 v[6:7], v[6:7], v[8:9]
	s_waitcnt vmcnt(0)
	v_lshlrev_b32_e32 v8, 16, v0
	v_and_b32_e32 v9, 0xffff0000, v0
	v_pk_add_f32 v[2:3], v[2:3], v[4:5]
	v_lshlrev_b32_e32 v0, 16, v1
	v_and_b32_e32 v1, 0xffff0000, v1
	v_pk_add_f32 v[70:71], v[6:7], v[8:9]
	v_pk_add_f32 v[68:69], v[2:3], v[0:1]
